# W_o units dealt to workgroups by XCD (4 row blocks x 8 column tiles per XCD) for L2 reuse of both operands
# speedup vs baseline: 1.0323x; 1.0039x over previous
; #define DENSE_UNIT(lds, cfg) gemm256dma_unit(lds, cfg)
; #define DENSE_UNIT(lds, cfg) gemm256_unit(lds, cfg)
;   for (int u = bid; u < 32 * 8; u += nb) {
;     const int uu = __builtin_amdgcn_readfirstlane(u);
;     CfgWo cfg{p, uu >> 3, uu & 7};
;     if (MODE == 0) DENSE_UNIT(lds, cfg); else gemm256_unit<CfgWo, MODE>(lds, cfg);
.LBB0_1260:
	s_or_b64 exec, exec, s[0:1]
	s_cmpk_gt_i32 s97, 0xff
	s_waitcnt lgkmcnt(0)
	s_barrier
	s_cbranch_scc1 .LBB0_1270
	v_readlane_b32 s4, v254, 39
	s_mov_b32 s47, 0x20000
	v_readlane_b32 s5, v254, 40
	v_readlane_b32 s6, v254, 41
	v_readlane_b32 s7, v254, 42
	v_readlane_b32 s8, v254, 43
	v_readlane_b32 s9, v254, 44
	v_readlane_b32 s10, v254, 45
	v_readlane_b32 s11, v254, 46
	s_mov_b32 s46, 0x800000
	s_and_b32 s45, s45, 0xffff
	s_brev_b32 s2, 64
	s_mov_b32 s3, s47
	s_and_b32 s1, s11, 0xffff
	s_movk_i32 s5, 0x63
	s_mov_b32 s6, 0
	s_mov_b32 s0, s10
	s_movk_i32 s7, 0x3c0
	s_movk_i32 s8, 0x80
	s_mov_b32 s4, 0x3f9837f0
	v_mov_b32_e32 v132, 1
	s_mov_b32 s9, s97
	s_and_b32 s99, s96, 7
	s_cmp_eq_u32 s99, 0
	s_cbranch_scc0 .Lwomap_keep
	s_and_b32 s9, s97, 7
	s_lshr_b32 s98, s96, 3
	s_mul_i32 s9, s9, s98
	s_lshr_b32 s98, s97, 3
	s_add_i32 s9, s9, s98
.Lwomap_keep:
	s_branch .LBB0_1263

; __global__ void __launch_bounds__(NTHREADS, 2) k_forward(Params p_in) {
	.amdhsa_kernel _Z9k_forward6Params
		.amdhsa_group_segment_fixed_size 0
		.amdhsa_private_segment_fixed_size 0
		.amdhsa_kernarg_size 712
		.amdhsa_user_sgpr_count 2
		.amdhsa_user_sgpr_dispatch_ptr 0
		.amdhsa_user_sgpr_queue_ptr 0
		.amdhsa_user_sgpr_kernarg_segment_ptr 1
		.amdhsa_user_sgpr_dispatch_id 0
		.amdhsa_user_sgpr_kernarg_preload_length 0
		.amdhsa_user_sgpr_kernarg_preload_offset 0
		.amdhsa_user_sgpr_private_segment_size 0
		.amdhsa_uses_dynamic_stack 0
		.amdhsa_enable_private_segment 0
		.amdhsa_system_sgpr_workgroup_id_x 1
		.amdhsa_system_sgpr_workgroup_id_y 0
		.amdhsa_system_sgpr_workgroup_id_z 0
		.amdhsa_system_sgpr_workgroup_info 0
		.amdhsa_system_vgpr_workitem_id 0
		.amdhsa_next_free_vgpr 256
		.amdhsa_next_free_sgpr 100
		.amdhsa_accum_offset 256
		.amdhsa_reserve_vcc 1
		.amdhsa_float_round_mode_32 0
		.amdhsa_float_round_mode_16_64 0
		.amdhsa_float_denorm_mode_32 3
		.amdhsa_float_denorm_mode_16_64 3
		.amdhsa_dx10_clamp 1
		.amdhsa_ieee_mode 1
		.amdhsa_fp16_overflow 0
		.amdhsa_tg_split 0
		.amdhsa_exception_fp_ieee_invalid_op 0
		.amdhsa_exception_fp_denorm_src 0
		.amdhsa_exception_fp_ieee_div_zero 0
		.amdhsa_exception_fp_ieee_overflow 0
		.amdhsa_exception_fp_ieee_underflow 0
		.amdhsa_exception_fp_ieee_inexact 0
		.amdhsa_exception_int_div_zero 0
	.end_amdhsa_kernel

; __global__ void __launch_bounds__(NTHREADS, 2) k_forward(Params p_in) {
amdhsa.kernels:
  - .agpr_count:     0
    .args:
      - .offset:         0
        .size:           456
        .value_kind:     by_value
      - .offset:         456
        .size:           4
        .value_kind:     hidden_block_count_x
      - .offset:         460
        .size:           4
        .value_kind:     hidden_block_count_y
      - .offset:         464
        .size:           4
        .value_kind:     hidden_block_count_z
      - .offset:         468
        .size:           2
        .value_kind:     hidden_group_size_x
      - .offset:         470
        .size:           2
        .value_kind:     hidden_group_size_y
      - .offset:         472
        .size:           2
        .value_kind:     hidden_group_size_z
      - .offset:         474
        .size:           2
        .value_kind:     hidden_remainder_x
      - .offset:         476
        .size:           2
        .value_kind:     hidden_remainder_y
      - .offset:         478
        .size:           2
        .value_kind:     hidden_remainder_z
      - .offset:         496
        .size:           8
        .value_kind:     hidden_global_offset_x
      - .offset:         504
        .size:           8
        .value_kind:     hidden_global_offset_y
      - .offset:         512
        .size:           8
        .value_kind:     hidden_global_offset_z
      - .offset:         520
        .size:           2
        .value_kind:     hidden_grid_dims
      - .offset:         576
        .size:           4
        .value_kind:     hidden_dynamic_lds_size
    .group_segment_fixed_size: 0
    .kernarg_segment_align: 8
    .kernarg_segment_size: 712
    .language:       OpenCL C
    .language_version:
      - 2
      - 0
    .max_flat_workgroup_size: 512
    .name:           _Z9k_forward6Params
    .private_segment_fixed_size: 0
    .sgpr_count:     106
    .sgpr_spill_count: 161
    .symbol:         _Z9k_forward6Params.kd
    .uniform_work_group_size: 1
    .uses_dynamic_stack: false
    .vgpr_count:     256
    .vgpr_spill_count: 0
    .wavefront_size: 64
